# v32 + at_dil QK step: bias-table LDS reads hoisted into the MFMA ladder (fresh registers), lgkmcnt waits regenerated
# speedup vs baseline: 1.0024x; 1.0024x over previous
; #define LAS __attribute__((address_space(3)))
; __device__ __forceinline__ int crow(int r, int hi) { return (r & 3) + 8 * (r >> 2) + 4 * hi; }
; __device__ __forceinline__ unsigned cvtpk(float lo, float hi) { f32x2_t v = {lo, hi}; bf16x2_t b = __builtin_convertvector(v, bf16x2_t); return __builtin_bit_cast(unsigned, b); }
; __device__ __forceinline__ void qkt(f32x16& p0, f32x16& p1, const LAS unsigned char* Kb, const bf16x8 (&qr)[4], float cinit, int r32, int hi) {
;     const int sw = (r32 >> 1) & 7;
;     bf16x8 kf[8];
; #pragma unroll
;     for (int d0 = 0; d0 < 4; ++d0) {
;         unsigned ka = (unsigned)(uintptr_t)Kb + r32 * 128 + (((2 * d0 + hi) ^ sw) << 4); asm volatile("" : "+v"(ka));
;         kf[2 * d0] = *(const LAS bf16x8*)(uintptr_t)ka;
;         kf[2 * d0 + 1] = *(const LAS bf16x8*)(uintptr_t)(ka + 4096);
;     }
; #pragma unroll
;     for (int r = 0; r < 16; ++r) { p0[r] = cinit; p1[r] = cinit; }
;     __builtin_amdgcn_sched_barrier(0);
; #pragma unroll
;     for (int d0 = 0; d0 < 4; ++d0) {
;         p0 = __builtin_amdgcn_mfma_f32_32x32x16_bf16(kf[2 * d0], qr[d0], p0, 0, 0, 0);
;         p1 = __builtin_amdgcn_mfma_f32_32x32x16_bf16(kf[2 * d0 + 1], qr[d0], p1, 0, 0, 0);
;     }
; __device__ __forceinline__ void at_dil(const Args& a, LAS unsigned char* lds, int layer) {
;     ...
;                 if (tt >= tt_lo) {
;                     f32x16 p0, p1;
;                     qkt(p0, p1, lds + L_K + tt * 8192, qr, -m_dil, r32, hi);
;                     const LAS float* tb = tab + (32 * wid + r32 + 192 - 64 * tt - 4 * hi - 63);
; #pragma unroll
;                     for (int r = 0; r < 16; ++r) { p0[r] += tb[63 - crow(r, 0)]; p1[r] += tb[31 - crow(r, 0)]; }
;                     exp_sum(p0, p1, l_part);
;                     pw[j][0] = (u32x4){cvtpk(p0[0], p0[1]), cvtpk(p0[2], p0[3]), cvtpk(p0[4], p0[5]), cvtpk(p0[6], p0[7])};
;                     pw[j][1] = (u32x4){cvtpk(p0[8], p0[9]), cvtpk(p0[10], p0[11]), cvtpk(p0[12], p0[13]), cvtpk(p0[14], p0[15])};
;                     pw[j][2] = (u32x4){cvtpk(p1[0], p1[1]), cvtpk(p1[2], p1[3]), cvtpk(p1[4], p1[5]), cvtpk(p1[6], p1[7])};
;                     pw[j][3] = (u32x4){cvtpk(p1[8], p1[9]), cvtpk(p1[10], p1[11]), cvtpk(p1[12], p1[13]), cvtpk(p1[14], p1[15])};
.LBB0_563:
	v_mov_b32_e32 v138, 0
	s_cmp_lt_i32 s42, s54
	v_lshlrev_b32_e32 v52, 2, v139
	s_cbranch_scc1 .LBB0_572
	s_nop 4
	v_add_u32_e32 v18, s46, v143
	v_add_u32_e32 v19, v144, v18
	ds_read_b128 v[36:39], v19
	ds_read_b128 v[54:57], v19 offset:4096
	v_add_u32_e32 v19, v142, v18
	ds_read_b128 v[58:61], v19
	ds_read_b128 v[62:65], v19 offset:4096
	v_add_u32_e32 v19, v141, v18
	v_add_u32_e32 v18, v140, v18
	ds_read_b128 v[88:91], v19
	ds_read_b128 v[96:99], v19 offset:4096
	ds_read_b128 v[104:107], v18
	ds_read_b128 v[112:115], v18 offset:4096
	s_waitcnt lgkmcnt(7)
	v_mfma_f32_32x32x16_bf16 v[18:33], v[36:39], v[68:71], v[2:17]
	v_add_lshl_u32 v53, v136, s43, 2
	v_add3_u32 v53, s73, v52, v53
	s_waitcnt lgkmcnt(6)
	v_mfma_f32_32x32x16_bf16 v[36:51], v[54:57], v[68:71], v[2:17]
	ds_read2_b32 v[162:163], v53 offset0:191 offset1:192
	ds_read2_b32 v[164:165], v53 offset0:189 offset1:190
	ds_read2_b32 v[166:167], v53 offset0:159 offset1:160
	ds_read2_b32 v[168:169], v53 offset0:157 offset1:158
	s_waitcnt lgkmcnt(9)
	v_mfma_f32_32x32x16_bf16 v[18:33], v[58:61], v[72:75], v[18:33]
	ds_read2_b32 v[170:171], v53 offset0:183 offset1:184
	ds_read2_b32 v[172:173], v53 offset0:181 offset1:182
	s_waitcnt lgkmcnt(10)
	v_mfma_f32_32x32x16_bf16 v[36:51], v[62:65], v[72:75], v[36:51]
	ds_read2_b32 v[174:175], v53 offset0:151 offset1:152
	ds_read2_b32 v[176:177], v53 offset0:149 offset1:150
	s_waitcnt lgkmcnt(11)
	v_mfma_f32_32x32x16_bf16 v[18:33], v[88:91], v[76:79], v[18:33]
	ds_read2_b32 v[178:179], v53 offset0:175 offset1:176
	ds_read2_b32 v[180:181], v53 offset0:173 offset1:174
	s_waitcnt lgkmcnt(12)
	v_mfma_f32_32x32x16_bf16 v[36:51], v[96:99], v[76:79], v[36:51]
	ds_read2_b32 v[182:183], v53 offset0:143 offset1:144
	ds_read2_b32 v[184:185], v53 offset0:141 offset1:142
	s_waitcnt lgkmcnt(13)
	v_mfma_f32_32x32x16_bf16 v[18:33], v[104:107], v[80:83], v[18:33]
	ds_read2_b32 v[186:187], v53 offset0:167 offset1:168
	s_waitcnt lgkmcnt(12)
	ds_read2_b32 v[188:189], v53 offset0:135 offset1:136
	v_mfma_f32_32x32x16_bf16 v[36:51], v[112:115], v[80:83], v[36:51]
	ds_read2_b32 v[190:191], v53 offset0:165 offset1:166
	s_waitcnt lgkmcnt(12)
	ds_read2_b32 v[192:193], v53 offset0:133 offset1:134
	s_nop 11
	v_add_f32_e32 v55, v18, v163
	v_add_f32_e32 v54, v19, v162
	v_add_f32_e32 v57, v20, v165
	v_add_f32_e32 v56, v21, v164
	v_exp_f32_e32 v55, v55
	v_add_f32_e32 v59, v36, v167
	v_add_f32_e32 v58, v37, v166
	s_waitcnt lgkmcnt(12)
	v_add_f32_e32 v61, v38, v169
	v_add_f32_e32 v60, v39, v168
	s_waitcnt lgkmcnt(11)
	v_add_f32_e32 v62, v22, v171
	s_waitcnt lgkmcnt(9)
	v_add_f32_e32 v37, v40, v175
	v_add_f32_e32 v40, v23, v170
	v_add_f32_e32 v36, v41, v174
	v_add_f32_e32 v41, v24, v173
	s_waitcnt lgkmcnt(8)
	v_add_f32_e32 v39, v42, v177
	v_add_f32_e32 v42, v25, v172
	v_add_f32_e32 v38, v43, v176
	s_waitcnt lgkmcnt(7)
	v_add_f32_e32 v43, v26, v179
	v_add_f32_e32 v63, v27, v178
	s_waitcnt lgkmcnt(5)
	v_add_f32_e32 v44, v44, v183
	v_add_f32_e32 v45, v45, v182
	v_add_f32_e32 v64, v28, v181
	v_add_f32_e32 v65, v29, v180
	v_exp_f32_e32 v59, v59
	s_waitcnt lgkmcnt(4)
	v_add_f32_e32 v46, v46, v185
	v_add_f32_e32 v47, v47, v184
	s_waitcnt lgkmcnt(3)
	v_add_f32_e32 v66, v30, v187
	s_waitcnt lgkmcnt(2)
	v_add_f32_e32 v48, v48, v189
	v_exp_f32_e32 v19, v54
	v_exp_f32_e32 v21, v58
	v_add_f32_e32 v53, v31, v186
	v_add_f32_e32 v49, v49, v188
	v_add_f32_e32 v18, v55, v59
	v_mov_b32_e32 v20, v35
	s_waitcnt lgkmcnt(1)
	v_add_f32_e32 v67, v32, v191
	v_add_f32_e32 v88, v33, v190
	v_exp_f32_e32 v54, v57
	v_exp_f32_e32 v57, v61
	v_pk_add_f32 v[22:23], v[18:19], v[20:21]
	v_exp_f32_e32 v18, v56
	s_waitcnt lgkmcnt(0)
	v_add_f32_e32 v50, v50, v193
	v_exp_f32_e32 v25, v60
	v_pk_add_f32 v[22:23], v[22:23], v[22:23] op_sel:[0,1] op_sel_hi:[1,0]
	v_add_f32_e32 v51, v51, v192
	v_add_f32_e32 v24, v54, v57
	v_mov_b32_e32 v23, v18
	v_exp_f32_e32 v20, v62
	v_exp_f32_e32 v56, v37
	v_pk_add_f32 v[22:23], v[22:23], v[24:25]
	v_exp_f32_e32 v24, v40
	v_exp_f32_e32 v27, v36
	v_pk_add_f32 v[22:23], v[22:23], v[22:23] op_sel:[0,1] op_sel_hi:[1,0]
	v_add_f32_e32 v26, v20, v56
	v_mov_b32_e32 v23, v24
	v_exp_f32_e32 v40, v41
	v_exp_f32_e32 v41, v39
	v_pk_add_f32 v[22:23], v[22:23], v[26:27]
	v_exp_f32_e32 v26, v42
	v_exp_f32_e32 v29, v38
	v_pk_add_f32 v[22:23], v[22:23], v[22:23] op_sel:[0,1] op_sel_hi:[1,0]
	v_add_f32_e32 v28, v40, v41
	v_mov_b32_e32 v23, v26
	v_exp_f32_e32 v42, v43
	v_exp_f32_e32 v43, v44
	v_pk_add_f32 v[22:23], v[22:23], v[28:29]
	v_exp_f32_e32 v28, v63
	v_exp_f32_e32 v31, v45
	v_pk_add_f32 v[22:23], v[22:23], v[22:23] op_sel:[0,1] op_sel_hi:[1,0]
	v_add_f32_e32 v30, v42, v43
	v_mov_b32_e32 v23, v28
	v_exp_f32_e32 v44, v64
	v_exp_f32_e32 v45, v46
	v_pk_add_f32 v[22:23], v[22:23], v[30:31]
	v_exp_f32_e32 v30, v65
	v_exp_f32_e32 v33, v47
	v_pk_add_f32 v[22:23], v[22:23], v[22:23] op_sel:[0,1] op_sel_hi:[1,0]
	v_add_f32_e32 v32, v44, v45
	v_mov_b32_e32 v23, v30
	v_exp_f32_e32 v46, v66
	v_exp_f32_e32 v47, v48
	v_pk_add_f32 v[22:23], v[22:23], v[32:33]
	v_exp_f32_e32 v32, v53
	v_exp_f32_e32 v37, v49
	v_pk_add_f32 v[22:23], v[22:23], v[22:23] op_sel:[0,1] op_sel_hi:[1,0]
	v_add_f32_e32 v36, v46, v47
	v_mov_b32_e32 v23, v32
	v_exp_f32_e32 v48, v67
	v_exp_f32_e32 v49, v50
	v_pk_add_f32 v[22:23], v[22:23], v[36:37]
	v_exp_f32_e32 v36, v88
	v_exp_f32_e32 v39, v51
	v_pk_add_f32 v[22:23], v[22:23], v[22:23] op_sel:[0,1] op_sel_hi:[1,0]
	v_add_f32_e32 v38, v48, v49
	v_mov_b32_e32 v23, v36
	v_pk_add_f32 v[22:23], v[22:23], v[38:39]
	v_cvt_pk_bf16_f32 v88, v55, v19
	v_add_f32_e32 v22, v22, v23
	v_add_f32_e32 v138, 0, v22
	v_cvt_pk_bf16_f32 v89, v54, v18
	v_cvt_pk_bf16_f32 v90, v20, v24
	v_cvt_pk_bf16_f32 v91, v40, v26
	v_cvt_pk_bf16_f32 v96, v42, v28
	v_cvt_pk_bf16_f32 v97, v44, v30
	v_cvt_pk_bf16_f32 v98, v46, v32
	v_cvt_pk_bf16_f32 v99, v48, v36
	v_cvt_pk_bf16_f32 v104, v59, v21
	v_cvt_pk_bf16_f32 v105, v57, v25
	v_cvt_pk_bf16_f32 v106, v56, v27
	v_cvt_pk_bf16_f32 v107, v41, v29
	v_cvt_pk_bf16_f32 v112, v43, v31
	v_cvt_pk_bf16_f32 v113, v45, v33
	v_cvt_pk_bf16_f32 v114, v47, v37
	v_cvt_pk_bf16_f32 v115, v49, v39
	s_cmp_lt_i32 s47, s54
	s_cbranch_scc1 .LBB0_574
	s_branch .LBB0_573
; #define LAS __attribute__((address_space(3)))
; __device__ __forceinline__ int crow(int r, int hi) { return (r & 3) + 8 * (r >> 2) + 4 * hi; }
; __device__ __forceinline__ void qkt(f32x16& p0, f32x16& p1, const LAS unsigned char* Kb, const bf16x8 (&qr)[4], float cinit, int r32, int hi) {
;     const int sw = (r32 >> 1) & 7;
;     bf16x8 kf[8];
; #pragma unroll
;     for (int d0 = 0; d0 < 4; ++d0) {
;         unsigned ka = (unsigned)(uintptr_t)Kb + r32 * 128 + (((2 * d0 + hi) ^ sw) << 4); asm volatile("" : "+v"(ka));
;         kf[2 * d0] = *(const LAS bf16x8*)(uintptr_t)ka;
;         kf[2 * d0 + 1] = *(const LAS bf16x8*)(uintptr_t)(ka + 4096);
;     }
; #pragma unroll
;     for (int r = 0; r < 16; ++r) { p0[r] = cinit; p1[r] = cinit; }
;     __builtin_amdgcn_sched_barrier(0);
; #pragma unroll
;     for (int d0 = 0; d0 < 4; ++d0) {
;         p0 = __builtin_amdgcn_mfma_f32_32x32x16_bf16(kf[2 * d0], qr[d0], p0, 0, 0, 0);
;         p1 = __builtin_amdgcn_mfma_f32_32x32x16_bf16(kf[2 * d0 + 1], qr[d0], p1, 0, 0, 0);
;     }
; __device__ __forceinline__ void at_dil(const Args& a, LAS unsigned char* lds, int layer) {
;     ...
;             mt = other_half_max(mt);
;             m_run = mt;
; #pragma unroll
;             for (int j = 0; j < 3; ++j) {
;                 const int tt = twlo + 2 - j;
;                 if (tt >= tt_lo) {
;                     f32x16 p0, p1;
;                     qkt(p0, p1, lds + L_K + tt * 8192, qr, -mt, r32, hi);
;                     const LAS float* tb = tab + (32 * wid + r32 + 192 - 64 * tt - 4 * hi - 63);
; #pragma unroll
;                     for (int r = 0; r < 16; ++r) { p0[r] += tb[63 - crow(r, 0)]; p1[r] += tb[31 - crow(r, 0)]; }
;                     exp_sum(p0, p1, l_part);
;                     pw[j][0] = (u32x4){cvtpk(p0[0], p0[1]), cvtpk(p0[2], p0[3]), cvtpk(p0[4], p0[5]), cvtpk(p0[6], p0[7])};
;                     pw[j][1] = (u32x4){cvtpk(p0[8], p0[9]), cvtpk(p0[10], p0[11]), cvtpk(p0[12], p0[13]), cvtpk(p0[14], p0[15])};
;                     pw[j][2] = (u32x4){cvtpk(p1[0], p1[1]), cvtpk(p1[2], p1[3]), cvtpk(p1[4], p1[5]), cvtpk(p1[6], p1[7])};
;                     pw[j][3] = (u32x4){cvtpk(p1[8], p1[9]), cvtpk(p1[10], p1[11]), cvtpk(p1[12], p1[13]), cvtpk(p1[14], p1[15])};
.LBB0_565:
	v_mov_b32_e32 v18, v58
	s_nop 1
	v_permlane32_swap_b32_e32 v58, v18
	v_max_f32_e32 v18, v18, v18
	v_max_f32_e32 v19, v58, v58
	v_max_f32_e32 v137, v19, v18
	v_xor_b32_e32 v18, 0x80000000, v137
	v_mov_b32_e32 v19, v18
	v_mov_b32_e32 v20, v18
	v_mov_b32_e32 v21, v18
	v_mov_b32_e32 v22, v18
	v_mov_b32_e32 v23, v18
	v_mov_b32_e32 v24, v18
	v_mov_b32_e32 v25, v18
	v_mov_b32_e32 v26, v18
	v_mov_b32_e32 v27, v18
	v_mov_b32_e32 v28, v18
	v_mov_b32_e32 v29, v18
	v_mov_b32_e32 v30, v18
	v_mov_b32_e32 v31, v18
	v_mov_b32_e32 v32, v18
	v_mov_b32_e32 v33, v18
	s_cmp_ge_i32 s42, s54
	v_mov_b32_e32 v138, 0
	s_cbranch_scc0 .LBB0_589
	v_add_u32_e32 v36, s46, v143
	v_add_u32_e32 v37, v144, v36
	ds_read_b128 v[52:55], v37
	ds_read_b128 v[88:91], v37 offset:4096
	v_add_u32_e32 v37, v142, v36
	ds_read_b128 v[96:99], v37
	ds_read_b128 v[104:107], v37 offset:4096
	v_add_u32_e32 v37, v141, v36
	v_add_u32_e32 v36, v140, v36
	ds_read_b128 v[112:115], v37
	ds_read_b128 v[146:149], v37 offset:4096
	ds_read_b128 v[150:153], v36
	ds_read_b128 v[154:157], v36 offset:4096
	s_waitcnt lgkmcnt(7)
	v_mfma_f32_32x32x16_bf16 v[36:51], v[52:55], v[68:71], v[18:33]
	s_waitcnt lgkmcnt(6)
	v_mfma_f32_32x32x16_bf16 v[52:67], v[88:91], v[68:71], v[18:33]
	v_lshlrev_b32_e32 v88, 2, v139
	v_add_lshl_u32 v89, v136, s43, 2
	s_waitcnt lgkmcnt(5)
	v_mfma_f32_32x32x16_bf16 v[36:51], v[96:99], v[72:75], v[36:51]
	s_waitcnt lgkmcnt(4)
	v_mfma_f32_32x32x16_bf16 v[52:67], v[104:107], v[72:75], v[52:67]
	v_add3_u32 v104, s73, v88, v89
	s_waitcnt lgkmcnt(3)
	v_mfma_f32_32x32x16_bf16 v[36:51], v[112:115], v[76:79], v[36:51]
	ds_read2_b32 v[162:163], v104 offset0:191 offset1:192
	ds_read2_b32 v[164:165], v104 offset0:189 offset1:190
	ds_read2_b32 v[166:167], v104 offset0:159 offset1:160
	ds_read2_b32 v[168:169], v104 offset0:157 offset1:158
	s_waitcnt lgkmcnt(6)
	v_mfma_f32_32x32x16_bf16 v[52:67], v[146:149], v[76:79], v[52:67]
	ds_read2_b32 v[170:171], v104 offset0:183 offset1:184
	ds_read2_b32 v[172:173], v104 offset0:181 offset1:182
	ds_read2_b32 v[174:175], v104 offset0:151 offset1:152
	ds_read2_b32 v[176:177], v104 offset0:149 offset1:150
	s_waitcnt lgkmcnt(9)
	v_mfma_f32_32x32x16_bf16 v[36:51], v[150:153], v[80:83], v[36:51]
	ds_read2_b32 v[178:179], v104 offset0:175 offset1:176
	ds_read2_b32 v[180:181], v104 offset0:173 offset1:174
	ds_read2_b32 v[182:183], v104 offset0:143 offset1:144
	ds_read2_b32 v[184:185], v104 offset0:141 offset1:142
	s_waitcnt lgkmcnt(12)
	v_mfma_f32_32x32x16_bf16 v[52:67], v[154:157], v[80:83], v[52:67]
	ds_read2_b32 v[186:187], v104 offset0:167 offset1:168
	ds_read2_b32 v[188:189], v104 offset0:135 offset1:136
	s_waitcnt lgkmcnt(12)
	ds_read2_b32 v[190:191], v104 offset0:165 offset1:166
	ds_read2_b32 v[192:193], v104 offset0:133 offset1:134
	s_nop 11
	v_add_f32_e32 v89, v36, v163
	v_add_f32_e32 v88, v37, v162
	v_add_f32_e32 v91, v38, v165
	v_add_f32_e32 v90, v39, v164
	v_exp_f32_e32 v89, v89
	s_waitcnt lgkmcnt(13)
	v_add_f32_e32 v97, v52, v167
	v_add_f32_e32 v96, v53, v166
	s_waitcnt lgkmcnt(12)
	v_add_f32_e32 v99, v54, v169
	v_add_f32_e32 v98, v55, v168
	s_waitcnt lgkmcnt(11)
	v_add_f32_e32 v105, v40, v171
	s_waitcnt lgkmcnt(9)
	v_add_f32_e32 v53, v56, v175
	v_add_f32_e32 v56, v41, v170
	v_add_f32_e32 v52, v57, v174
	v_add_f32_e32 v57, v42, v173
	s_waitcnt lgkmcnt(8)
	v_add_f32_e32 v55, v58, v177
	v_add_f32_e32 v58, v43, v172
	v_add_f32_e32 v54, v59, v176
	s_waitcnt lgkmcnt(7)
	v_add_f32_e32 v59, v44, v179
	v_add_f32_e32 v106, v45, v178
	s_waitcnt lgkmcnt(5)
	v_add_f32_e32 v60, v60, v183
	v_add_f32_e32 v61, v61, v182
	v_add_f32_e32 v107, v46, v181
	v_add_f32_e32 v112, v47, v180
	v_exp_f32_e32 v145, v97
	s_waitcnt lgkmcnt(4)
	v_add_f32_e32 v62, v62, v185
	v_add_f32_e32 v63, v63, v184
	s_waitcnt lgkmcnt(3)
	v_add_f32_e32 v113, v48, v187
	s_waitcnt lgkmcnt(2)
	v_add_f32_e32 v64, v64, v189
	v_exp_f32_e32 v37, v88
	v_exp_f32_e32 v39, v96
	v_add_f32_e32 v104, v49, v186
	v_add_f32_e32 v65, v65, v188
	v_add_f32_e32 v36, v89, v145
	v_mov_b32_e32 v38, v35
	s_waitcnt lgkmcnt(1)
	v_add_f32_e32 v114, v50, v191
	v_add_f32_e32 v115, v51, v190
	v_exp_f32_e32 v91, v91
	v_exp_f32_e32 v146, v99
	v_pk_add_f32 v[40:41], v[36:37], v[38:39]
	v_exp_f32_e32 v36, v90
	s_waitcnt lgkmcnt(0)
	v_add_f32_e32 v66, v66, v193
	v_exp_f32_e32 v43, v98
	v_pk_add_f32 v[40:41], v[40:41], v[40:41] op_sel:[0,1] op_sel_hi:[1,0]
	v_add_f32_e32 v67, v67, v192
	v_add_f32_e32 v42, v91, v146
	v_mov_b32_e32 v41, v36
	v_exp_f32_e32 v38, v105
	v_exp_f32_e32 v147, v53
	v_pk_add_f32 v[40:41], v[40:41], v[42:43]
	v_exp_f32_e32 v42, v56
	v_exp_f32_e32 v45, v52
	v_pk_add_f32 v[40:41], v[40:41], v[40:41] op_sel:[0,1] op_sel_hi:[1,0]
	v_add_f32_e32 v44, v38, v147
	v_mov_b32_e32 v41, v42
	v_exp_f32_e32 v56, v57
	v_exp_f32_e32 v57, v55
	v_pk_add_f32 v[40:41], v[40:41], v[44:45]
	v_exp_f32_e32 v44, v58
	v_exp_f32_e32 v47, v54
	v_pk_add_f32 v[40:41], v[40:41], v[40:41] op_sel:[0,1] op_sel_hi:[1,0]
	v_add_f32_e32 v46, v56, v57
	v_mov_b32_e32 v41, v44
	v_exp_f32_e32 v58, v59
	v_exp_f32_e32 v59, v60
	v_pk_add_f32 v[40:41], v[40:41], v[46:47]
	v_exp_f32_e32 v46, v106
	v_exp_f32_e32 v49, v61
	v_pk_add_f32 v[40:41], v[40:41], v[40:41] op_sel:[0,1] op_sel_hi:[1,0]
	v_add_f32_e32 v48, v58, v59
	v_mov_b32_e32 v41, v46
	v_exp_f32_e32 v60, v107
	v_exp_f32_e32 v61, v62
	v_pk_add_f32 v[40:41], v[40:41], v[48:49]
	v_exp_f32_e32 v48, v112
	v_exp_f32_e32 v51, v63
	v_pk_add_f32 v[40:41], v[40:41], v[40:41] op_sel:[0,1] op_sel_hi:[1,0]
	v_add_f32_e32 v50, v60, v61
	v_mov_b32_e32 v41, v48
	v_exp_f32_e32 v62, v113
	v_exp_f32_e32 v63, v64
	v_pk_add_f32 v[40:41], v[40:41], v[50:51]
	v_exp_f32_e32 v50, v104
	v_exp_f32_e32 v53, v65
	v_pk_add_f32 v[40:41], v[40:41], v[40:41] op_sel:[0,1] op_sel_hi:[1,0]
	v_add_f32_e32 v52, v62, v63
	v_mov_b32_e32 v41, v50
	v_exp_f32_e32 v64, v114
	v_exp_f32_e32 v65, v66
	v_pk_add_f32 v[40:41], v[40:41], v[52:53]
	v_exp_f32_e32 v52, v115
	v_exp_f32_e32 v55, v67
	v_pk_add_f32 v[40:41], v[40:41], v[40:41] op_sel:[0,1] op_sel_hi:[1,0]
	v_add_f32_e32 v54, v64, v65
	v_mov_b32_e32 v41, v52
	v_pk_add_f32 v[40:41], v[40:41], v[54:55]
	v_cvt_pk_bf16_f32 v88, v89, v37
	v_add_f32_e32 v40, v40, v41
	v_add_f32_e32 v138, 0, v40
	v_cvt_pk_bf16_f32 v89, v91, v36
	v_cvt_pk_bf16_f32 v90, v38, v42
	v_cvt_pk_bf16_f32 v91, v56, v44
	v_cvt_pk_bf16_f32 v96, v58, v46
	v_cvt_pk_bf16_f32 v97, v60, v48
	v_cvt_pk_bf16_f32 v98, v62, v50
	v_cvt_pk_bf16_f32 v99, v64, v52
	v_cvt_pk_bf16_f32 v104, v145, v39
	v_cvt_pk_bf16_f32 v105, v146, v43
	v_cvt_pk_bf16_f32 v106, v147, v45
	v_cvt_pk_bf16_f32 v107, v57, v47
	v_cvt_pk_bf16_f32 v112, v59, v49
	v_cvt_pk_bf16_f32 v113, v61, v51
	v_cvt_pk_bf16_f32 v114, v63, v53
	v_cvt_pk_bf16_f32 v115, v65, v55
	s_cmp_lt_i32 s47, s54
	s_cbranch_scc0 .LBB0_590

; #define LAS __attribute__((address_space(3)))
; __device__ __forceinline__ int crow(int r, int hi) { return (r & 3) + 8 * (r >> 2) + 4 * hi; }
; __device__ __forceinline__ unsigned cvtpk(float lo, float hi) { f32x2_t v = {lo, hi}; bf16x2_t b = __builtin_convertvector(v, bf16x2_t); return __builtin_bit_cast(unsigned, b); }
; __device__ __forceinline__ void exp_sum(f32x16& p0, f32x16& p1, float& l_part) {
;     float rs = 0.f;
; #pragma unroll
;     for (int r = 0; r < 16; ++r) { p0[r] = __builtin_amdgcn_exp2f(p0[r]); p1[r] = __builtin_amdgcn_exp2f(p1[r]); rs += p0[r] + p1[r]; }
;     l_part += rs;
; __device__ __forceinline__ void at_dil(const Args& a, LAS unsigned char* lds, int layer) {
;     ...
;             for (int j = 0; j < 3; ++j) {
;                 const int tt = twlo + 2 - j;
;                 if (tt >= tt_lo) {
;                     f32x16 p0, p1;
;                     qkt(p0, p1, lds + L_K + tt * 8192, qr, -m_dil, r32, hi);
;                     const LAS float* tb = tab + (32 * wid + r32 + 192 - 64 * tt - 4 * hi - 63);
; #pragma unroll
;                     for (int r = 0; r < 16; ++r) { p0[r] += tb[63 - crow(r, 0)]; p1[r] += tb[31 - crow(r, 0)]; }
;                     exp_sum(p0, p1, l_part);
;                     pw[j][0] = (u32x4){cvtpk(p0[0], p0[1]), cvtpk(p0[2], p0[3]), cvtpk(p0[4], p0[5]), cvtpk(p0[6], p0[7])};
;                     pw[j][1] = (u32x4){cvtpk(p0[8], p0[9]), cvtpk(p0[10], p0[11]), cvtpk(p0[12], p0[13]), cvtpk(p0[14], p0[15])};
;                     pw[j][2] = (u32x4){cvtpk(p1[0], p1[1]), cvtpk(p1[2], p1[3]), cvtpk(p1[4], p1[5]), cvtpk(p1[6], p1[7])};
;                     pw[j][3] = (u32x4){cvtpk(p1[8], p1[9]), cvtpk(p1[10], p1[11]), cvtpk(p1[12], p1[13]), cvtpk(p1[14], p1[15])};
.LBB0_573:
	s_nop 2
	v_add_u32_e32 v18, s48, v143
	v_add_u32_e32 v19, v144, v18
	ds_read_b128 v[36:39], v19
	ds_read_b128 v[54:57], v19 offset:4096
	v_add_u32_e32 v19, v142, v18
	ds_read_b128 v[58:61], v19
	ds_read_b128 v[62:65], v19 offset:4096
	v_add_u32_e32 v19, v141, v18
	v_add_u32_e32 v18, v140, v18
	ds_read_b128 v[84:87], v19
	ds_read_b128 v[92:95], v19 offset:4096
	ds_read_b128 v[100:103], v18
	ds_read_b128 v[108:111], v18 offset:4096
	s_waitcnt lgkmcnt(7)
	v_mfma_f32_32x32x16_bf16 v[18:33], v[36:39], v[68:71], v[2:17]
	v_add_lshl_u32 v53, v136, s43, 2
	s_waitcnt lgkmcnt(6)
	v_mfma_f32_32x32x16_bf16 v[36:51], v[54:57], v[68:71], v[2:17]
	s_waitcnt lgkmcnt(5)
	v_mfma_f32_32x32x16_bf16 v[18:33], v[58:61], v[72:75], v[18:33]
	v_add3_u32 v60, s75, v52, v53
	s_waitcnt lgkmcnt(4)
	v_mfma_f32_32x32x16_bf16 v[36:51], v[62:65], v[72:75], v[36:51]
	ds_read2_b32 v[162:163], v60 offset0:191 offset1:192
	ds_read2_b32 v[164:165], v60 offset0:189 offset1:190
	ds_read2_b32 v[166:167], v60 offset0:159 offset1:160
	ds_read2_b32 v[168:169], v60 offset0:157 offset1:158
	s_waitcnt lgkmcnt(7)
	v_mfma_f32_32x32x16_bf16 v[18:33], v[84:87], v[76:79], v[18:33]
	ds_read2_b32 v[170:171], v60 offset0:183 offset1:184
	ds_read2_b32 v[172:173], v60 offset0:181 offset1:182
	ds_read2_b32 v[174:175], v60 offset0:151 offset1:152
	ds_read2_b32 v[176:177], v60 offset0:149 offset1:150
	s_waitcnt lgkmcnt(10)
	v_mfma_f32_32x32x16_bf16 v[36:51], v[92:95], v[76:79], v[36:51]
	ds_read2_b32 v[178:179], v60 offset0:175 offset1:176
	ds_read2_b32 v[180:181], v60 offset0:173 offset1:174
	ds_read2_b32 v[182:183], v60 offset0:143 offset1:144
	ds_read2_b32 v[184:185], v60 offset0:141 offset1:142
	s_waitcnt lgkmcnt(13)
	v_mfma_f32_32x32x16_bf16 v[18:33], v[100:103], v[80:83], v[18:33]
	ds_read2_b32 v[186:187], v60 offset0:167 offset1:168
	s_waitcnt lgkmcnt(12)
	ds_read2_b32 v[188:189], v60 offset0:135 offset1:136
	v_mfma_f32_32x32x16_bf16 v[36:51], v[108:111], v[80:83], v[36:51]
	ds_read2_b32 v[190:191], v60 offset0:165 offset1:166
	s_waitcnt lgkmcnt(12)
	ds_read2_b32 v[192:193], v60 offset0:133 offset1:134
	s_nop 11
	v_add_f32_e32 v53, v18, v163
	v_add_f32_e32 v52, v19, v162
	v_add_f32_e32 v55, v20, v165
	v_add_f32_e32 v54, v21, v164
	v_exp_f32_e32 v53, v53
	v_add_f32_e32 v57, v36, v167
	v_add_f32_e32 v56, v37, v166
	s_waitcnt lgkmcnt(12)
	v_add_f32_e32 v59, v38, v169
	v_add_f32_e32 v58, v39, v168
	s_waitcnt lgkmcnt(11)
	v_add_f32_e32 v61, v22, v171
	s_waitcnt lgkmcnt(9)
	v_add_f32_e32 v37, v40, v175
	v_add_f32_e32 v40, v23, v170
	v_add_f32_e32 v36, v41, v174
	v_add_f32_e32 v41, v24, v173
	s_waitcnt lgkmcnt(8)
	v_add_f32_e32 v39, v42, v177
	v_add_f32_e32 v42, v25, v172
	v_add_f32_e32 v38, v43, v176
	s_waitcnt lgkmcnt(7)
	v_add_f32_e32 v43, v26, v179
	v_add_f32_e32 v62, v27, v178
	s_waitcnt lgkmcnt(5)
	v_add_f32_e32 v44, v44, v183
	v_add_f32_e32 v45, v45, v182
	v_add_f32_e32 v63, v28, v181
	v_add_f32_e32 v64, v29, v180
	v_exp_f32_e32 v57, v57
	s_waitcnt lgkmcnt(4)
	v_add_f32_e32 v46, v46, v185
	v_add_f32_e32 v47, v47, v184
	s_waitcnt lgkmcnt(3)
	v_add_f32_e32 v65, v30, v187
	s_waitcnt lgkmcnt(2)
	v_add_f32_e32 v48, v48, v189
	v_exp_f32_e32 v19, v52
	v_exp_f32_e32 v21, v56
	v_add_f32_e32 v60, v31, v186
	v_add_f32_e32 v49, v49, v188
	v_add_f32_e32 v18, v53, v57
	v_mov_b32_e32 v20, v35
	s_waitcnt lgkmcnt(1)
	v_add_f32_e32 v66, v32, v191
	v_add_f32_e32 v67, v33, v190
	v_exp_f32_e32 v52, v55
	v_exp_f32_e32 v55, v59
	v_pk_add_f32 v[22:23], v[18:19], v[20:21]
	v_exp_f32_e32 v18, v54
	s_waitcnt lgkmcnt(0)
	v_add_f32_e32 v50, v50, v193
	v_exp_f32_e32 v25, v58
	v_pk_add_f32 v[22:23], v[22:23], v[22:23] op_sel:[0,1] op_sel_hi:[1,0]
	v_add_f32_e32 v51, v51, v192
	v_add_f32_e32 v24, v52, v55
	v_mov_b32_e32 v23, v18
	v_exp_f32_e32 v20, v61
	v_exp_f32_e32 v54, v37
	v_pk_add_f32 v[22:23], v[22:23], v[24:25]
	v_exp_f32_e32 v24, v40
	v_exp_f32_e32 v27, v36
	v_pk_add_f32 v[22:23], v[22:23], v[22:23] op_sel:[0,1] op_sel_hi:[1,0]
	v_add_f32_e32 v26, v20, v54
	v_mov_b32_e32 v23, v24
	v_exp_f32_e32 v40, v41
	v_exp_f32_e32 v41, v39
	v_pk_add_f32 v[22:23], v[22:23], v[26:27]
	v_exp_f32_e32 v26, v42
	v_exp_f32_e32 v29, v38
	v_pk_add_f32 v[22:23], v[22:23], v[22:23] op_sel:[0,1] op_sel_hi:[1,0]
	v_add_f32_e32 v28, v40, v41
	v_mov_b32_e32 v23, v26
	v_exp_f32_e32 v42, v43
	v_exp_f32_e32 v43, v44
	v_pk_add_f32 v[22:23], v[22:23], v[28:29]
	v_exp_f32_e32 v28, v62
	v_exp_f32_e32 v31, v45
	v_pk_add_f32 v[22:23], v[22:23], v[22:23] op_sel:[0,1] op_sel_hi:[1,0]
	v_add_f32_e32 v30, v42, v43
	v_mov_b32_e32 v23, v28
	v_exp_f32_e32 v44, v63
	v_exp_f32_e32 v45, v46
	v_pk_add_f32 v[22:23], v[22:23], v[30:31]
	v_exp_f32_e32 v30, v64
	v_exp_f32_e32 v33, v47
	v_pk_add_f32 v[22:23], v[22:23], v[22:23] op_sel:[0,1] op_sel_hi:[1,0]
	v_add_f32_e32 v32, v44, v45
	v_mov_b32_e32 v23, v30
	v_exp_f32_e32 v46, v65
	v_exp_f32_e32 v47, v48
	v_pk_add_f32 v[22:23], v[22:23], v[32:33]
	v_exp_f32_e32 v32, v60
	v_exp_f32_e32 v37, v49
	v_pk_add_f32 v[22:23], v[22:23], v[22:23] op_sel:[0,1] op_sel_hi:[1,0]
	v_add_f32_e32 v36, v46, v47
	v_mov_b32_e32 v23, v32
	v_exp_f32_e32 v48, v66
	v_exp_f32_e32 v49, v50
	v_pk_add_f32 v[22:23], v[22:23], v[36:37]
	v_exp_f32_e32 v36, v67
	v_exp_f32_e32 v39, v51
	v_pk_add_f32 v[22:23], v[22:23], v[22:23] op_sel:[0,1] op_sel_hi:[1,0]
	v_add_f32_e32 v38, v48, v49
	v_mov_b32_e32 v23, v36
	v_pk_add_f32 v[22:23], v[22:23], v[38:39]
	v_cvt_pk_bf16_f32 v84, v53, v19
	v_add_f32_e32 v22, v22, v23
	v_add_f32_e32 v138, v138, v22
	v_cvt_pk_bf16_f32 v85, v52, v18
	v_cvt_pk_bf16_f32 v86, v20, v24
	v_cvt_pk_bf16_f32 v87, v40, v26
	v_cvt_pk_bf16_f32 v92, v42, v28
	v_cvt_pk_bf16_f32 v93, v44, v30
	v_cvt_pk_bf16_f32 v94, v46, v32
	v_cvt_pk_bf16_f32 v95, v48, v36
	v_cvt_pk_bf16_f32 v100, v57, v21
	v_cvt_pk_bf16_f32 v101, v55, v25
	v_cvt_pk_bf16_f32 v102, v54, v27
	v_cvt_pk_bf16_f32 v103, v41, v29
	v_cvt_pk_bf16_f32 v108, v43, v31
	v_cvt_pk_bf16_f32 v109, v45, v33
	v_cvt_pk_bf16_f32 v110, v47, v37
	v_cvt_pk_bf16_f32 v111, v49, v39
